# selection pass 1 rewritten: k >= (bl<<21) compare, exec set from vcc, count recovered from the append pointer (5-7 instr per key instead of 9-13)
# speedup vs baseline: 1.0111x; 1.0111x over previous
; #define LAS __attribute__((address_space(3)))
; __device__ __forceinline__ bool dsa2_sampled(LAS unsigned char* wl, const unsigned (&kk)[128], int nreg, int n, int lane) {
;     ...
;     int cur = 0; LAS unsigned* pp = (LAS unsigned*)(PRIV + lane);
; #pragma unroll
;     for (int i = 0; i < 128; ++i) { if ((i & ~15) < nreg) { const unsigned k = kk[i];
;             if ((k >> 21) >= bl) { if (cur < 24) { pp[0] = (unsigned)(lane + 64 * i); pp[1] = k; } pp += 128; ++cur; } }
;         __builtin_amdgcn_sched_barrier(0); }
.LBB0_763:
	s_waitcnt lgkmcnt(0)
	v_min_u32_e32 v0, v168, v2
	v_lshl_add_u32 v6, v129, 3, s57
	s_mov_b64 s[0:1], exec
	v_lshlrev_b32_e32 v0, 21, v0
	v_mov_b32_e32 v1, v6
	v_add_u32_e32 v5, 0x2e00, v6
	v_cmp_ge_u32_e32 vcc, v166, v0
	s_mov_b64 exec, vcc
	ds_write2_b32 v1, v129, v166 offset1:1
	v_add_u32_e32 v1, 0x200, v1
	s_mov_b64 exec, s[0:1]
	v_cmp_ge_u32_e32 vcc, v165, v0
	v_or_b32_e32 v4, 0x40, v129
	s_mov_b64 exec, vcc
	ds_write2_b32 v1, v4, v165 offset1:1
	v_add_u32_e32 v1, 0x200, v1
	s_mov_b64 exec, s[0:1]
	v_cmp_ge_u32_e32 vcc, v164, v0
	v_or_b32_e32 v4, 0x80, v129
	s_mov_b64 exec, vcc
	ds_write2_b32 v1, v4, v164 offset1:1
	v_add_u32_e32 v1, 0x200, v1
	s_mov_b64 exec, s[0:1]
	v_cmp_ge_u32_e32 vcc, v163, v0
	v_or_b32_e32 v4, 0xc0, v129
	s_mov_b64 exec, vcc
	ds_write2_b32 v1, v4, v163 offset1:1
	v_add_u32_e32 v1, 0x200, v1
	s_mov_b64 exec, s[0:1]
	v_cmp_ge_u32_e32 vcc, v162, v0
	v_or_b32_e32 v4, 0x100, v129
	s_mov_b64 exec, vcc
	ds_write2_b32 v1, v4, v162 offset1:1
	v_add_u32_e32 v1, 0x200, v1
	s_mov_b64 exec, s[0:1]
	v_cmp_ge_u32_e32 vcc, v161, v0
	v_or_b32_e32 v4, 0x140, v129
	s_mov_b64 exec, vcc
	ds_write2_b32 v1, v4, v161 offset1:1
	v_add_u32_e32 v1, 0x200, v1
	s_mov_b64 exec, s[0:1]
	v_cmp_ge_u32_e32 vcc, v160, v0
	v_or_b32_e32 v4, 0x180, v129
	s_mov_b64 exec, vcc
	ds_write2_b32 v1, v4, v160 offset1:1
	v_add_u32_e32 v1, 0x200, v1
	s_mov_b64 exec, s[0:1]
	v_cmp_ge_u32_e32 vcc, v159, v0
	v_or_b32_e32 v4, 0x1c0, v129
	s_mov_b64 exec, vcc
	ds_write2_b32 v1, v4, v159 offset1:1
	v_add_u32_e32 v1, 0x200, v1
	s_mov_b64 exec, s[0:1]
	v_cmp_ge_u32_e32 vcc, v158, v0
	v_or_b32_e32 v4, 0x200, v129
	s_mov_b64 exec, vcc
	ds_write2_b32 v1, v4, v158 offset1:1
	v_add_u32_e32 v1, 0x200, v1
	s_mov_b64 exec, s[0:1]
	v_cmp_ge_u32_e32 vcc, v157, v0
	v_or_b32_e32 v4, 0x240, v129
	s_mov_b64 exec, vcc
	ds_write2_b32 v1, v4, v157 offset1:1
	v_add_u32_e32 v1, 0x200, v1
	s_mov_b64 exec, s[0:1]
	v_cmp_ge_u32_e32 vcc, v155, v0
	v_or_b32_e32 v4, 0x280, v129
	s_mov_b64 exec, vcc
	ds_write2_b32 v1, v4, v155 offset1:1
	v_add_u32_e32 v1, 0x200, v1
	s_mov_b64 exec, s[0:1]
	v_cmp_ge_u32_e32 vcc, v154, v0
	v_or_b32_e32 v4, 0x2c0, v129
	s_mov_b64 exec, vcc
	ds_write2_b32 v1, v4, v154 offset1:1
	v_add_u32_e32 v1, 0x200, v1
	s_mov_b64 exec, s[0:1]
	v_cmp_ge_u32_e32 vcc, v153, v0
	v_or_b32_e32 v4, 0x300, v129
	s_mov_b64 exec, vcc
	ds_write2_b32 v1, v4, v153 offset1:1
	v_add_u32_e32 v1, 0x200, v1
	s_mov_b64 exec, s[0:1]
	v_cmp_ge_u32_e32 vcc, v152, v0
	v_or_b32_e32 v4, 0x340, v129
	s_mov_b64 exec, vcc
	ds_write2_b32 v1, v4, v152 offset1:1
	v_add_u32_e32 v1, 0x200, v1
	s_mov_b64 exec, s[0:1]
	v_cmp_ge_u32_e32 vcc, v151, v0
	v_or_b32_e32 v4, 0x380, v129
	s_mov_b64 exec, vcc
	ds_write2_b32 v1, v4, v151 offset1:1
	v_add_u32_e32 v1, 0x200, v1
	s_mov_b64 exec, s[0:1]
	v_cmp_ge_u32_e32 vcc, v149, v0
	v_or_b32_e32 v4, 0x3c0, v129
	s_mov_b64 exec, vcc
	ds_write2_b32 v1, v4, v149 offset1:1
	v_add_u32_e32 v1, 0x200, v1
	s_mov_b64 exec, s[0:1]
	v_cmp_ge_u32_e32 vcc, v148, v0
	v_or_b32_e32 v4, 0x400, v129
	s_mov_b64 exec, vcc
	ds_write2_b32 v1, v4, v148 offset1:1
	v_add_u32_e32 v1, 0x200, v1
	s_mov_b64 exec, s[0:1]
	v_cmp_ge_u32_e32 vcc, v147, v0
	v_or_b32_e32 v4, 0x440, v129
	s_mov_b64 exec, vcc
	ds_write2_b32 v1, v4, v147 offset1:1
	v_add_u32_e32 v1, 0x200, v1
	s_mov_b64 exec, s[0:1]
	v_cmp_ge_u32_e32 vcc, v146, v0
	v_or_b32_e32 v4, 0x480, v129
	s_mov_b64 exec, vcc
	ds_write2_b32 v1, v4, v146 offset1:1
	v_add_u32_e32 v1, 0x200, v1
	s_mov_b64 exec, s[0:1]
	v_cmp_ge_u32_e32 vcc, v145, v0
	v_or_b32_e32 v4, 0x4c0, v129
	s_mov_b64 exec, vcc
	ds_write2_b32 v1, v4, v145 offset1:1
	v_add_u32_e32 v1, 0x200, v1
	s_mov_b64 exec, s[0:1]
	v_cmp_ge_u32_e32 vcc, v144, v0
	v_or_b32_e32 v4, 0x500, v129
	s_mov_b64 exec, vcc
	ds_write2_b32 v1, v4, v144 offset1:1
	v_add_u32_e32 v1, 0x200, v1
	s_mov_b64 exec, s[0:1]
	v_cmp_ge_u32_e32 vcc, v143, v0
	v_or_b32_e32 v4, 0x540, v129
	s_mov_b64 exec, vcc
	ds_write2_b32 v1, v4, v143 offset1:1
	v_add_u32_e32 v1, 0x200, v1
	s_mov_b64 exec, s[0:1]
	v_cmp_ge_u32_e32 vcc, v142, v0
	v_or_b32_e32 v4, 0x580, v129
	s_mov_b64 exec, vcc
	ds_write2_b32 v1, v4, v142 offset1:1
	v_add_u32_e32 v1, 0x200, v1
	s_mov_b64 exec, s[0:1]
	v_cmp_ge_u32_e32 vcc, v141, v0
	v_or_b32_e32 v4, 0x5c0, v129
	s_mov_b64 exec, vcc
	ds_write2_b32 v1, v4, v141 offset1:1
	v_add_u32_e32 v1, 0x200, v1
	s_mov_b64 exec, s[0:1]
	v_cmp_ge_u32_e32 vcc, v140, v0
	v_or_b32_e32 v4, 0x600, v129
	v_min_u32_e32 v3, v1, v5
	s_mov_b64 exec, vcc
	ds_write2_b32 v3, v4, v140 offset1:1
	v_add_u32_e32 v1, 0x200, v1
	s_mov_b64 exec, s[0:1]
	v_cmp_ge_u32_e32 vcc, v139, v0
	v_or_b32_e32 v4, 0x640, v129
	v_min_u32_e32 v3, v1, v5
	s_mov_b64 exec, vcc
	ds_write2_b32 v3, v4, v139 offset1:1
	v_add_u32_e32 v1, 0x200, v1
	s_mov_b64 exec, s[0:1]
	v_cmp_ge_u32_e32 vcc, v137, v0
	v_or_b32_e32 v4, 0x680, v129
	v_min_u32_e32 v3, v1, v5
	s_mov_b64 exec, vcc
	ds_write2_b32 v3, v4, v137 offset1:1
	v_add_u32_e32 v1, 0x200, v1
	s_mov_b64 exec, s[0:1]
	v_cmp_ge_u32_e32 vcc, v136, v0
	v_or_b32_e32 v4, 0x6c0, v129
	v_min_u32_e32 v3, v1, v5
	s_mov_b64 exec, vcc
	ds_write2_b32 v3, v4, v136 offset1:1
	v_add_u32_e32 v1, 0x200, v1
	s_mov_b64 exec, s[0:1]
	v_cmp_ge_u32_e32 vcc, v134, v0
	v_or_b32_e32 v4, 0x700, v129
	v_min_u32_e32 v3, v1, v5
	s_mov_b64 exec, vcc
	ds_write2_b32 v3, v4, v134 offset1:1
	v_add_u32_e32 v1, 0x200, v1
	s_mov_b64 exec, s[0:1]
	v_cmp_ge_u32_e32 vcc, v132, v0
	v_or_b32_e32 v4, 0x740, v129
	v_min_u32_e32 v3, v1, v5
	s_mov_b64 exec, vcc
	ds_write2_b32 v3, v4, v132 offset1:1
	v_add_u32_e32 v1, 0x200, v1
	s_mov_b64 exec, s[0:1]
	v_cmp_ge_u32_e32 vcc, v130, v0
	v_or_b32_e32 v4, 0x780, v129
	v_min_u32_e32 v3, v1, v5
; #define LAS __attribute__((address_space(3)))
; __device__ __forceinline__ bool dsa2_sampled(LAS unsigned char* wl, const unsigned (&kk)[128], int nreg, int n, int lane) {
;     ...
;     int cur = 0; LAS unsigned* pp = (LAS unsigned*)(PRIV + lane);
; #pragma unroll
;     for (int i = 0; i < 128; ++i) { if ((i & ~15) < nreg) { const unsigned k = kk[i];
;             if ((k >> 21) >= bl) { if (cur < 24) { pp[0] = (unsigned)(lane + 64 * i); pp[1] = k; } pp += 128; ++cur; } }
;         __builtin_amdgcn_sched_barrier(0); }
	s_mov_b64 exec, vcc
	ds_write2_b32 v3, v4, v130 offset1:1
	v_add_u32_e32 v1, 0x200, v1
	s_mov_b64 exec, s[0:1]
	v_cmp_ge_u32_e32 vcc, v126, v0
	v_or_b32_e32 v4, 0x7c0, v129
	v_min_u32_e32 v3, v1, v5
	s_mov_b64 exec, vcc
	ds_write2_b32 v3, v4, v126 offset1:1
	v_add_u32_e32 v1, 0x200, v1
	s_mov_b64 exec, s[0:1]
	v_cmp_ge_u32_e32 vcc, v135, v0
	v_or_b32_e32 v4, 0x800, v129
	v_min_u32_e32 v3, v1, v5
	s_mov_b64 exec, vcc
	ds_write2_b32 v3, v4, v135 offset1:1
	v_add_u32_e32 v1, 0x200, v1
	s_mov_b64 exec, s[0:1]
	v_cmp_ge_u32_e32 vcc, v133, v0
	v_or_b32_e32 v4, 0x840, v129
	v_min_u32_e32 v3, v1, v5
	s_mov_b64 exec, vcc
	ds_write2_b32 v3, v4, v133 offset1:1
	v_add_u32_e32 v1, 0x200, v1
	s_mov_b64 exec, s[0:1]
	v_cmp_ge_u32_e32 vcc, v131, v0
	v_or_b32_e32 v4, 0x880, v129
	v_min_u32_e32 v3, v1, v5
	s_mov_b64 exec, vcc
	ds_write2_b32 v3, v4, v131 offset1:1
	v_add_u32_e32 v1, 0x200, v1
	s_mov_b64 exec, s[0:1]
	v_cmp_ge_u32_e32 vcc, v127, v0
	v_or_b32_e32 v4, 0x8c0, v129
	v_min_u32_e32 v3, v1, v5
	s_mov_b64 exec, vcc
	ds_write2_b32 v3, v4, v127 offset1:1
	v_add_u32_e32 v1, 0x200, v1
	s_mov_b64 exec, s[0:1]
	v_cmp_ge_u32_e32 vcc, v125, v0
	v_or_b32_e32 v4, 0x900, v129
	v_min_u32_e32 v3, v1, v5
	s_mov_b64 exec, vcc
	ds_write2_b32 v3, v4, v125 offset1:1
	v_add_u32_e32 v1, 0x200, v1
	s_mov_b64 exec, s[0:1]
	v_cmp_ge_u32_e32 vcc, v124, v0
	v_or_b32_e32 v4, 0x940, v129
	v_min_u32_e32 v3, v1, v5
	s_mov_b64 exec, vcc
	ds_write2_b32 v3, v4, v124 offset1:1
	v_add_u32_e32 v1, 0x200, v1
	s_mov_b64 exec, s[0:1]
	v_cmp_ge_u32_e32 vcc, v123, v0
	v_or_b32_e32 v4, 0x980, v129
	v_min_u32_e32 v3, v1, v5
	s_mov_b64 exec, vcc
	ds_write2_b32 v3, v4, v123 offset1:1
	v_add_u32_e32 v1, 0x200, v1
	s_mov_b64 exec, s[0:1]
	v_cmp_ge_u32_e32 vcc, v122, v0
	v_or_b32_e32 v4, 0x9c0, v129
	v_min_u32_e32 v3, v1, v5
	s_mov_b64 exec, vcc
	ds_write2_b32 v3, v4, v122 offset1:1
	v_add_u32_e32 v1, 0x200, v1
	s_mov_b64 exec, s[0:1]
	v_cmp_ge_u32_e32 vcc, v121, v0
	v_or_b32_e32 v4, 0xa00, v129
	v_min_u32_e32 v3, v1, v5
	s_mov_b64 exec, vcc
	ds_write2_b32 v3, v4, v121 offset1:1
	v_add_u32_e32 v1, 0x200, v1
	s_mov_b64 exec, s[0:1]
	v_cmp_ge_u32_e32 vcc, v120, v0
	v_or_b32_e32 v4, 0xa40, v129
	v_min_u32_e32 v3, v1, v5
	s_mov_b64 exec, vcc
	ds_write2_b32 v3, v4, v120 offset1:1
	v_add_u32_e32 v1, 0x200, v1
	s_mov_b64 exec, s[0:1]
	v_cmp_ge_u32_e32 vcc, v119, v0
	v_or_b32_e32 v4, 0xa80, v129
	v_min_u32_e32 v3, v1, v5
	s_mov_b64 exec, vcc
	ds_write2_b32 v3, v4, v119 offset1:1
	v_add_u32_e32 v1, 0x200, v1
	s_mov_b64 exec, s[0:1]
	v_cmp_ge_u32_e32 vcc, v118, v0
	v_or_b32_e32 v4, 0xac0, v129
	v_min_u32_e32 v3, v1, v5
	s_mov_b64 exec, vcc
	ds_write2_b32 v3, v4, v118 offset1:1
	v_add_u32_e32 v1, 0x200, v1
	s_mov_b64 exec, s[0:1]
	v_cmp_ge_u32_e32 vcc, v117, v0
	v_or_b32_e32 v4, 0xb00, v129
	v_min_u32_e32 v3, v1, v5
	s_mov_b64 exec, vcc
	ds_write2_b32 v3, v4, v117 offset1:1
	v_add_u32_e32 v1, 0x200, v1
	s_mov_b64 exec, s[0:1]
	v_cmp_ge_u32_e32 vcc, v116, v0
	v_or_b32_e32 v4, 0xb40, v129
	v_min_u32_e32 v3, v1, v5
	s_mov_b64 exec, vcc
	ds_write2_b32 v3, v4, v116 offset1:1
	v_add_u32_e32 v1, 0x200, v1
	s_mov_b64 exec, s[0:1]
	v_cmp_ge_u32_e32 vcc, v115, v0
	v_or_b32_e32 v4, 0xb80, v129
	v_min_u32_e32 v3, v1, v5
	s_mov_b64 exec, vcc
	ds_write2_b32 v3, v4, v115 offset1:1
	v_add_u32_e32 v1, 0x200, v1
	s_mov_b64 exec, s[0:1]
	v_cmp_ge_u32_e32 vcc, v114, v0
	v_or_b32_e32 v4, 0xbc0, v129
	v_min_u32_e32 v3, v1, v5
	s_mov_b64 exec, vcc
	ds_write2_b32 v3, v4, v114 offset1:1
	v_add_u32_e32 v1, 0x200, v1
	s_mov_b64 exec, s[0:1]
	v_cmp_ge_u32_e32 vcc, v113, v0
	v_or_b32_e32 v4, 0xc00, v129
	v_min_u32_e32 v3, v1, v5
	s_mov_b64 exec, vcc
	ds_write2_b32 v3, v4, v113 offset1:1
	v_add_u32_e32 v1, 0x200, v1
	s_mov_b64 exec, s[0:1]
	v_cmp_ge_u32_e32 vcc, v112, v0
	v_or_b32_e32 v4, 0xc40, v129
	v_min_u32_e32 v3, v1, v5
	s_mov_b64 exec, vcc
	ds_write2_b32 v3, v4, v112 offset1:1
	v_add_u32_e32 v1, 0x200, v1
	s_mov_b64 exec, s[0:1]
	v_cmp_ge_u32_e32 vcc, v111, v0
	v_or_b32_e32 v4, 0xc80, v129
	v_min_u32_e32 v3, v1, v5
	s_mov_b64 exec, vcc
	ds_write2_b32 v3, v4, v111 offset1:1
	v_add_u32_e32 v1, 0x200, v1
	s_mov_b64 exec, s[0:1]
	v_cmp_ge_u32_e32 vcc, v110, v0
	v_or_b32_e32 v4, 0xcc0, v129
	v_min_u32_e32 v3, v1, v5
	s_mov_b64 exec, vcc
	ds_write2_b32 v3, v4, v110 offset1:1
	v_add_u32_e32 v1, 0x200, v1
	s_mov_b64 exec, s[0:1]
	v_cmp_ge_u32_e32 vcc, v109, v0
	v_or_b32_e32 v4, 0xd00, v129
	v_min_u32_e32 v3, v1, v5
	s_mov_b64 exec, vcc
	ds_write2_b32 v3, v4, v109 offset1:1
	v_add_u32_e32 v1, 0x200, v1
	s_mov_b64 exec, s[0:1]
	v_cmp_ge_u32_e32 vcc, v108, v0
	v_or_b32_e32 v4, 0xd40, v129
	v_min_u32_e32 v3, v1, v5
	s_mov_b64 exec, vcc
	ds_write2_b32 v3, v4, v108 offset1:1
	v_add_u32_e32 v1, 0x200, v1
	s_mov_b64 exec, s[0:1]
	v_cmp_ge_u32_e32 vcc, v107, v0
	v_or_b32_e32 v4, 0xd80, v129
	v_min_u32_e32 v3, v1, v5
	s_mov_b64 exec, vcc
	ds_write2_b32 v3, v4, v107 offset1:1
	v_add_u32_e32 v1, 0x200, v1
	s_mov_b64 exec, s[0:1]
	v_cmp_ge_u32_e32 vcc, v106, v0
	v_or_b32_e32 v4, 0xdc0, v129
	v_min_u32_e32 v3, v1, v5
	s_mov_b64 exec, vcc
	ds_write2_b32 v3, v4, v106 offset1:1
	v_add_u32_e32 v1, 0x200, v1
	s_mov_b64 exec, s[0:1]
	v_cmp_ge_u32_e32 vcc, v105, v0
	v_or_b32_e32 v4, 0xe00, v129
	v_min_u32_e32 v3, v1, v5
	s_mov_b64 exec, vcc
	ds_write2_b32 v3, v4, v105 offset1:1
	v_add_u32_e32 v1, 0x200, v1
	s_mov_b64 exec, s[0:1]
	v_cmp_ge_u32_e32 vcc, v104, v0
	v_or_b32_e32 v4, 0xe40, v129
	v_min_u32_e32 v3, v1, v5
	s_mov_b64 exec, vcc
	ds_write2_b32 v3, v4, v104 offset1:1
	v_add_u32_e32 v1, 0x200, v1
	s_mov_b64 exec, s[0:1]
	v_cmp_ge_u32_e32 vcc, v103, v0
	v_or_b32_e32 v4, 0xe80, v129
	v_min_u32_e32 v3, v1, v5
	s_mov_b64 exec, vcc
; #define LAS __attribute__((address_space(3)))
; __device__ __forceinline__ bool dsa2_sampled(LAS unsigned char* wl, const unsigned (&kk)[128], int nreg, int n, int lane) {
;     ...
;     int cur = 0; LAS unsigned* pp = (LAS unsigned*)(PRIV + lane);
; #pragma unroll
;     for (int i = 0; i < 128; ++i) { if ((i & ~15) < nreg) { const unsigned k = kk[i];
;             if ((k >> 21) >= bl) { if (cur < 24) { pp[0] = (unsigned)(lane + 64 * i); pp[1] = k; } pp += 128; ++cur; } }
;         __builtin_amdgcn_sched_barrier(0); }
	ds_write2_b32 v3, v4, v103 offset1:1
	v_add_u32_e32 v1, 0x200, v1
	s_mov_b64 exec, s[0:1]
	v_cmp_ge_u32_e32 vcc, v102, v0
	v_or_b32_e32 v4, 0xec0, v129
	v_min_u32_e32 v3, v1, v5
	s_mov_b64 exec, vcc
	ds_write2_b32 v3, v4, v102 offset1:1
	v_add_u32_e32 v1, 0x200, v1
	s_mov_b64 exec, s[0:1]
	v_cmp_ge_u32_e32 vcc, v100, v0
	v_or_b32_e32 v4, 0xf00, v129
	v_min_u32_e32 v3, v1, v5
	s_mov_b64 exec, vcc
	ds_write2_b32 v3, v4, v100 offset1:1
	v_add_u32_e32 v1, 0x200, v1
	s_mov_b64 exec, s[0:1]
	v_cmp_ge_u32_e32 vcc, v98, v0
	v_or_b32_e32 v4, 0xf40, v129
	v_min_u32_e32 v3, v1, v5
	s_mov_b64 exec, vcc
	ds_write2_b32 v3, v4, v98 offset1:1
	v_add_u32_e32 v1, 0x200, v1
	s_mov_b64 exec, s[0:1]
	v_cmp_ge_u32_e32 vcc, v96, v0
	v_or_b32_e32 v4, 0xf80, v129
	v_min_u32_e32 v3, v1, v5
	s_mov_b64 exec, vcc
	ds_write2_b32 v3, v4, v96 offset1:1
	v_add_u32_e32 v1, 0x200, v1
	s_mov_b64 exec, s[0:1]
	v_cmp_ge_u32_e32 vcc, v94, v0
	v_or_b32_e32 v4, 0xfc0, v129
	v_min_u32_e32 v3, v1, v5
	s_mov_b64 exec, vcc
	ds_write2_b32 v3, v4, v94 offset1:1
	v_add_u32_e32 v1, 0x200, v1
	s_mov_b64 exec, s[0:1]
	v_cmp_ge_u32_e32 vcc, v101, v0
	v_or_b32_e32 v4, 0x1000, v129
	v_min_u32_e32 v3, v1, v5
	s_mov_b64 exec, vcc
	ds_write2_b32 v3, v4, v101 offset1:1
	v_add_u32_e32 v1, 0x200, v1
	s_mov_b64 exec, s[0:1]
	v_cmp_ge_u32_e32 vcc, v99, v0
	v_or_b32_e32 v4, 0x1040, v129
	v_min_u32_e32 v3, v1, v5
	s_mov_b64 exec, vcc
	ds_write2_b32 v3, v4, v99 offset1:1
	v_add_u32_e32 v1, 0x200, v1
	s_mov_b64 exec, s[0:1]
	v_cmp_ge_u32_e32 vcc, v97, v0
	v_or_b32_e32 v4, 0x1080, v129
	v_min_u32_e32 v3, v1, v5
	s_mov_b64 exec, vcc
	ds_write2_b32 v3, v4, v97 offset1:1
	v_add_u32_e32 v1, 0x200, v1
	s_mov_b64 exec, s[0:1]
	v_cmp_ge_u32_e32 vcc, v95, v0
	v_or_b32_e32 v4, 0x10c0, v129
	v_min_u32_e32 v3, v1, v5
	s_mov_b64 exec, vcc
	ds_write2_b32 v3, v4, v95 offset1:1
	v_add_u32_e32 v1, 0x200, v1
	s_mov_b64 exec, s[0:1]
	v_cmp_ge_u32_e32 vcc, v93, v0
	v_or_b32_e32 v4, 0x1100, v129
	v_min_u32_e32 v3, v1, v5
	s_mov_b64 exec, vcc
	ds_write2_b32 v3, v4, v93 offset1:1
	v_add_u32_e32 v1, 0x200, v1
	s_mov_b64 exec, s[0:1]
	v_cmp_ge_u32_e32 vcc, v92, v0
	v_or_b32_e32 v4, 0x1140, v129
	v_min_u32_e32 v3, v1, v5
	s_mov_b64 exec, vcc
	ds_write2_b32 v3, v4, v92 offset1:1
	v_add_u32_e32 v1, 0x200, v1
	s_mov_b64 exec, s[0:1]
	v_cmp_ge_u32_e32 vcc, v91, v0
	v_or_b32_e32 v4, 0x1180, v129
	v_min_u32_e32 v3, v1, v5
	s_mov_b64 exec, vcc
	ds_write2_b32 v3, v4, v91 offset1:1
	v_add_u32_e32 v1, 0x200, v1
	s_mov_b64 exec, s[0:1]
	v_cmp_ge_u32_e32 vcc, v90, v0
	v_or_b32_e32 v4, 0x11c0, v129
	v_min_u32_e32 v3, v1, v5
	s_mov_b64 exec, vcc
	ds_write2_b32 v3, v4, v90 offset1:1
	v_add_u32_e32 v1, 0x200, v1
	s_mov_b64 exec, s[0:1]
	v_cmp_ge_u32_e32 vcc, v89, v0
	v_or_b32_e32 v4, 0x1200, v129
	v_min_u32_e32 v3, v1, v5
	s_mov_b64 exec, vcc
	ds_write2_b32 v3, v4, v89 offset1:1
	v_add_u32_e32 v1, 0x200, v1
	s_mov_b64 exec, s[0:1]
	v_cmp_ge_u32_e32 vcc, v88, v0
	v_or_b32_e32 v4, 0x1240, v129
	v_min_u32_e32 v3, v1, v5
	s_mov_b64 exec, vcc
	ds_write2_b32 v3, v4, v88 offset1:1
	v_add_u32_e32 v1, 0x200, v1
	s_mov_b64 exec, s[0:1]
	v_cmp_ge_u32_e32 vcc, v87, v0
	v_or_b32_e32 v4, 0x1280, v129
	v_min_u32_e32 v3, v1, v5
	s_mov_b64 exec, vcc
	ds_write2_b32 v3, v4, v87 offset1:1
	v_add_u32_e32 v1, 0x200, v1
	s_mov_b64 exec, s[0:1]
	v_cmp_ge_u32_e32 vcc, v86, v0
	v_or_b32_e32 v4, 0x12c0, v129
	v_min_u32_e32 v3, v1, v5
	s_mov_b64 exec, vcc
	ds_write2_b32 v3, v4, v86 offset1:1
	v_add_u32_e32 v1, 0x200, v1
	s_mov_b64 exec, s[0:1]
	v_cmp_ge_u32_e32 vcc, v85, v0
	v_or_b32_e32 v4, 0x1300, v129
	v_min_u32_e32 v3, v1, v5
	s_mov_b64 exec, vcc
	ds_write2_b32 v3, v4, v85 offset1:1
	v_add_u32_e32 v1, 0x200, v1
	s_mov_b64 exec, s[0:1]
	v_cmp_ge_u32_e32 vcc, v84, v0
	v_or_b32_e32 v4, 0x1340, v129
	v_min_u32_e32 v3, v1, v5
	s_mov_b64 exec, vcc
	ds_write2_b32 v3, v4, v84 offset1:1
	v_add_u32_e32 v1, 0x200, v1
	s_mov_b64 exec, s[0:1]
	v_cmp_ge_u32_e32 vcc, v83, v0
	v_or_b32_e32 v4, 0x1380, v129
	v_min_u32_e32 v3, v1, v5
	s_mov_b64 exec, vcc
	ds_write2_b32 v3, v4, v83 offset1:1
	v_add_u32_e32 v1, 0x200, v1
	s_mov_b64 exec, s[0:1]
	v_cmp_ge_u32_e32 vcc, v82, v0
	v_or_b32_e32 v4, 0x13c0, v129
	v_min_u32_e32 v3, v1, v5
	s_mov_b64 exec, vcc
	ds_write2_b32 v3, v4, v82 offset1:1
	v_add_u32_e32 v1, 0x200, v1
	s_mov_b64 exec, s[0:1]
	v_cmp_ge_u32_e32 vcc, v81, v0
	v_or_b32_e32 v4, 0x1400, v129
	v_min_u32_e32 v3, v1, v5
	s_mov_b64 exec, vcc
	ds_write2_b32 v3, v4, v81 offset1:1
	v_add_u32_e32 v1, 0x200, v1
	s_mov_b64 exec, s[0:1]
	v_cmp_ge_u32_e32 vcc, v80, v0
	v_or_b32_e32 v4, 0x1440, v129
	v_min_u32_e32 v3, v1, v5
	s_mov_b64 exec, vcc
	ds_write2_b32 v3, v4, v80 offset1:1
	v_add_u32_e32 v1, 0x200, v1
	s_mov_b64 exec, s[0:1]
	v_cmp_ge_u32_e32 vcc, v79, v0
	v_or_b32_e32 v4, 0x1480, v129
	v_min_u32_e32 v3, v1, v5
	s_mov_b64 exec, vcc
	ds_write2_b32 v3, v4, v79 offset1:1
	v_add_u32_e32 v1, 0x200, v1
	s_mov_b64 exec, s[0:1]
	v_cmp_ge_u32_e32 vcc, v78, v0
	v_or_b32_e32 v4, 0x14c0, v129
	v_min_u32_e32 v3, v1, v5
	s_mov_b64 exec, vcc
	ds_write2_b32 v3, v4, v78 offset1:1
	v_add_u32_e32 v1, 0x200, v1
	s_mov_b64 exec, s[0:1]
	v_cmp_ge_u32_e32 vcc, v77, v0
	v_or_b32_e32 v4, 0x1500, v129
	v_min_u32_e32 v3, v1, v5
	s_mov_b64 exec, vcc
	ds_write2_b32 v3, v4, v77 offset1:1
	v_add_u32_e32 v1, 0x200, v1
	s_mov_b64 exec, s[0:1]
	v_cmp_ge_u32_e32 vcc, v76, v0
	v_or_b32_e32 v4, 0x1540, v129
	v_min_u32_e32 v3, v1, v5
	s_mov_b64 exec, vcc
	ds_write2_b32 v3, v4, v76 offset1:1
	v_add_u32_e32 v1, 0x200, v1
	s_mov_b64 exec, s[0:1]
	v_cmp_ge_u32_e32 vcc, v75, v0
	v_or_b32_e32 v4, 0x1580, v129
	v_min_u32_e32 v3, v1, v5
	s_mov_b64 exec, vcc
	ds_write2_b32 v3, v4, v75 offset1:1
	v_add_u32_e32 v1, 0x200, v1
; #define LAS __attribute__((address_space(3)))
; __device__ __forceinline__ bool dsa2_sampled(LAS unsigned char* wl, const unsigned (&kk)[128], int nreg, int n, int lane) {
;     ...
;     int cur = 0; LAS unsigned* pp = (LAS unsigned*)(PRIV + lane);
; #pragma unroll
;     for (int i = 0; i < 128; ++i) { if ((i & ~15) < nreg) { const unsigned k = kk[i];
;             if ((k >> 21) >= bl) { if (cur < 24) { pp[0] = (unsigned)(lane + 64 * i); pp[1] = k; } pp += 128; ++cur; } }
;         __builtin_amdgcn_sched_barrier(0); }
	s_mov_b64 exec, s[0:1]
	v_cmp_ge_u32_e32 vcc, v74, v0
	v_or_b32_e32 v4, 0x15c0, v129
	v_min_u32_e32 v3, v1, v5
	s_mov_b64 exec, vcc
	ds_write2_b32 v3, v4, v74 offset1:1
	v_add_u32_e32 v1, 0x200, v1
	s_mov_b64 exec, s[0:1]
	v_cmp_ge_u32_e32 vcc, v73, v0
	v_or_b32_e32 v4, 0x1600, v129
	v_min_u32_e32 v3, v1, v5
	s_mov_b64 exec, vcc
	ds_write2_b32 v3, v4, v73 offset1:1
	v_add_u32_e32 v1, 0x200, v1
	s_mov_b64 exec, s[0:1]
	v_cmp_ge_u32_e32 vcc, v72, v0
	v_or_b32_e32 v4, 0x1640, v129
	v_min_u32_e32 v3, v1, v5
	s_mov_b64 exec, vcc
	ds_write2_b32 v3, v4, v72 offset1:1
	v_add_u32_e32 v1, 0x200, v1
	s_mov_b64 exec, s[0:1]
	v_cmp_ge_u32_e32 vcc, v71, v0
	v_or_b32_e32 v4, 0x1680, v129
	v_min_u32_e32 v3, v1, v5
	s_mov_b64 exec, vcc
	ds_write2_b32 v3, v4, v71 offset1:1
	v_add_u32_e32 v1, 0x200, v1
	s_mov_b64 exec, s[0:1]
	v_cmp_ge_u32_e32 vcc, v70, v0
	v_or_b32_e32 v4, 0x16c0, v129
	v_min_u32_e32 v3, v1, v5
	s_mov_b64 exec, vcc
	ds_write2_b32 v3, v4, v70 offset1:1
	v_add_u32_e32 v1, 0x200, v1
	s_mov_b64 exec, s[0:1]
	v_cmp_ge_u32_e32 vcc, v68, v0
	v_or_b32_e32 v4, 0x1700, v129
	v_min_u32_e32 v3, v1, v5
	s_mov_b64 exec, vcc
	ds_write2_b32 v3, v4, v68 offset1:1
	v_add_u32_e32 v1, 0x200, v1
	s_mov_b64 exec, s[0:1]
	v_cmp_ge_u32_e32 vcc, v66, v0
	v_or_b32_e32 v4, 0x1740, v129
	v_min_u32_e32 v3, v1, v5
	s_mov_b64 exec, vcc
	ds_write2_b32 v3, v4, v66 offset1:1
	v_add_u32_e32 v1, 0x200, v1
	s_mov_b64 exec, s[0:1]
	v_cmp_ge_u32_e32 vcc, v64, v0
	v_or_b32_e32 v4, 0x1780, v129
	v_min_u32_e32 v3, v1, v5
	s_mov_b64 exec, vcc
	ds_write2_b32 v3, v4, v64 offset1:1
	v_add_u32_e32 v1, 0x200, v1
	s_mov_b64 exec, s[0:1]
	v_cmp_ge_u32_e32 vcc, v57, v0
	v_or_b32_e32 v4, 0x17c0, v129
	v_min_u32_e32 v3, v1, v5
	s_mov_b64 exec, vcc
	ds_write2_b32 v3, v4, v57 offset1:1
	v_add_u32_e32 v1, 0x200, v1
	s_mov_b64 exec, s[0:1]
	v_cmp_ge_u32_e32 vcc, v69, v0
	v_or_b32_e32 v4, 0x1800, v129
	v_min_u32_e32 v3, v1, v5
	s_mov_b64 exec, vcc
	ds_write2_b32 v3, v4, v69 offset1:1
	v_add_u32_e32 v1, 0x200, v1
	s_mov_b64 exec, s[0:1]
	v_cmp_ge_u32_e32 vcc, v67, v0
	v_or_b32_e32 v4, 0x1840, v129
	v_min_u32_e32 v3, v1, v5
	s_mov_b64 exec, vcc
	ds_write2_b32 v3, v4, v67 offset1:1
	v_add_u32_e32 v1, 0x200, v1
	s_mov_b64 exec, s[0:1]
	v_cmp_ge_u32_e32 vcc, v65, v0
	v_or_b32_e32 v4, 0x1880, v129
	v_min_u32_e32 v3, v1, v5
	s_mov_b64 exec, vcc
	ds_write2_b32 v3, v4, v65 offset1:1
	v_add_u32_e32 v1, 0x200, v1
	s_mov_b64 exec, s[0:1]
	v_cmp_ge_u32_e32 vcc, v63, v0
	v_or_b32_e32 v4, 0x18c0, v129
	v_min_u32_e32 v3, v1, v5
	s_mov_b64 exec, vcc
	ds_write2_b32 v3, v4, v63 offset1:1
	v_add_u32_e32 v1, 0x200, v1
	s_mov_b64 exec, s[0:1]
	v_cmp_ge_u32_e32 vcc, v62, v0
	v_or_b32_e32 v4, 0x1900, v129
	v_min_u32_e32 v3, v1, v5
	s_mov_b64 exec, vcc
	ds_write2_b32 v3, v4, v62 offset1:1
	v_add_u32_e32 v1, 0x200, v1
	s_mov_b64 exec, s[0:1]
	v_cmp_ge_u32_e32 vcc, v61, v0
	v_or_b32_e32 v4, 0x1940, v129
	v_min_u32_e32 v3, v1, v5
	s_mov_b64 exec, vcc
	ds_write2_b32 v3, v4, v61 offset1:1
	v_add_u32_e32 v1, 0x200, v1
	s_mov_b64 exec, s[0:1]
	v_cmp_ge_u32_e32 vcc, v60, v0
	v_or_b32_e32 v4, 0x1980, v129
	v_min_u32_e32 v3, v1, v5
	s_mov_b64 exec, vcc
	ds_write2_b32 v3, v4, v60 offset1:1
	v_add_u32_e32 v1, 0x200, v1
	s_mov_b64 exec, s[0:1]
	v_cmp_ge_u32_e32 vcc, v59, v0
	v_or_b32_e32 v4, 0x19c0, v129
	v_min_u32_e32 v3, v1, v5
	s_mov_b64 exec, vcc
	ds_write2_b32 v3, v4, v59 offset1:1
	v_add_u32_e32 v1, 0x200, v1
	s_mov_b64 exec, s[0:1]
	v_cmp_ge_u32_e32 vcc, v58, v0
	v_or_b32_e32 v4, 0x1a00, v129
	v_min_u32_e32 v3, v1, v5
	s_mov_b64 exec, vcc
	ds_write2_b32 v3, v4, v58 offset1:1
	v_add_u32_e32 v1, 0x200, v1
	s_mov_b64 exec, s[0:1]
	v_cmp_ge_u32_e32 vcc, v56, v0
	v_or_b32_e32 v4, 0x1a40, v129
	v_min_u32_e32 v3, v1, v5
	s_mov_b64 exec, vcc
	ds_write2_b32 v3, v4, v56 offset1:1
	v_add_u32_e32 v1, 0x200, v1
	s_mov_b64 exec, s[0:1]
	v_cmp_ge_u32_e32 vcc, v55, v0
	v_or_b32_e32 v4, 0x1a80, v129
	v_min_u32_e32 v3, v1, v5
	s_mov_b64 exec, vcc
	ds_write2_b32 v3, v4, v55 offset1:1
	v_add_u32_e32 v1, 0x200, v1
	s_mov_b64 exec, s[0:1]
	v_cmp_ge_u32_e32 vcc, v54, v0
	v_or_b32_e32 v4, 0x1ac0, v129
	v_min_u32_e32 v3, v1, v5
	s_mov_b64 exec, vcc
	ds_write2_b32 v3, v4, v54 offset1:1
	v_add_u32_e32 v1, 0x200, v1
	s_mov_b64 exec, s[0:1]
	v_cmp_ge_u32_e32 vcc, v53, v0
	v_or_b32_e32 v4, 0x1b00, v129
	v_min_u32_e32 v3, v1, v5
	s_mov_b64 exec, vcc
	ds_write2_b32 v3, v4, v53 offset1:1
	v_add_u32_e32 v1, 0x200, v1
	s_mov_b64 exec, s[0:1]
	v_cmp_ge_u32_e32 vcc, v52, v0
	v_or_b32_e32 v4, 0x1b40, v129
	v_min_u32_e32 v3, v1, v5
	s_mov_b64 exec, vcc
	ds_write2_b32 v3, v4, v52 offset1:1
	v_add_u32_e32 v1, 0x200, v1
; #define LAS __attribute__((address_space(3)))
; #define LDS_WAIT() asm volatile("s_waitcnt lgkmcnt(0)" ::: "memory")
; __device__ __forceinline__ int lane_op() { int l = (int)__builtin_amdgcn_mbcnt_hi(~0u, __builtin_amdgcn_mbcnt_lo(~0u, 0u)); asm volatile("" : "+v"(l)); return l; }
; #define SHX(v, m, l) bperm_((l) ^ (m), (v))
; __device__ __forceinline__ bool dsa2_sampled(LAS unsigned char* wl, const unsigned (&kk)[128], int nreg, int n, int lane) {
;     ...
;     int cur = 0; LAS unsigned* pp = (LAS unsigned*)(PRIV + lane);
; #pragma unroll
;     for (int i = 0; i < 128; ++i) { if ((i & ~15) < nreg) { const unsigned k = kk[i];
;             if ((k >> 21) >= bl) { if (cur < 24) { pp[0] = (unsigned)(lane + 64 * i); pp[1] = k; } pp += 128; ++cur; } }
;         __builtin_amdgcn_sched_barrier(0); }
;     LDS_WAIT();
;     int mxc = cur; { const int lq_ = lane_op();
; #pragma unroll
;         for (int o = 1; o < 64; o <<= 1) { const int t2 = SHX(mxc, o, lq_); mxc = t2 > mxc ? t2 : mxc; } }
;     mxc = __builtin_amdgcn_readfirstlane(mxc);
	s_mov_b64 exec, s[0:1]
	v_cmp_ge_u32_e32 vcc, v51, v0
	v_or_b32_e32 v4, 0x1b80, v129
	v_min_u32_e32 v3, v1, v5
	s_mov_b64 exec, vcc
	ds_write2_b32 v3, v4, v51 offset1:1
	v_add_u32_e32 v1, 0x200, v1
	s_mov_b64 exec, s[0:1]
	v_cmp_ge_u32_e32 vcc, v50, v0
	v_or_b32_e32 v4, 0x1bc0, v129
	v_min_u32_e32 v3, v1, v5
	s_mov_b64 exec, vcc
	ds_write2_b32 v3, v4, v50 offset1:1
	v_add_u32_e32 v1, 0x200, v1
	s_mov_b64 exec, s[0:1]
	v_cmp_ge_u32_e32 vcc, v49, v0
	v_or_b32_e32 v4, 0x1c00, v129
	v_min_u32_e32 v3, v1, v5
	s_mov_b64 exec, vcc
	ds_write2_b32 v3, v4, v49 offset1:1
	v_add_u32_e32 v1, 0x200, v1
	s_mov_b64 exec, s[0:1]
	v_cmp_ge_u32_e32 vcc, v48, v0
	v_or_b32_e32 v4, 0x1c40, v129
	v_min_u32_e32 v3, v1, v5
	s_mov_b64 exec, vcc
	ds_write2_b32 v3, v4, v48 offset1:1
	v_add_u32_e32 v1, 0x200, v1
	s_mov_b64 exec, s[0:1]
	v_cmp_ge_u32_e32 vcc, v47, v0
	v_or_b32_e32 v4, 0x1c80, v129
	v_min_u32_e32 v3, v1, v5
	s_mov_b64 exec, vcc
	ds_write2_b32 v3, v4, v47 offset1:1
	v_add_u32_e32 v1, 0x200, v1
	s_mov_b64 exec, s[0:1]
	v_cmp_ge_u32_e32 vcc, v46, v0
	v_or_b32_e32 v4, 0x1cc0, v129
	v_min_u32_e32 v3, v1, v5
	s_mov_b64 exec, vcc
	ds_write2_b32 v3, v4, v46 offset1:1
	v_add_u32_e32 v1, 0x200, v1
	s_mov_b64 exec, s[0:1]
	v_cmp_ge_u32_e32 vcc, v45, v0
	v_or_b32_e32 v4, 0x1d00, v129
	v_min_u32_e32 v3, v1, v5
	s_mov_b64 exec, vcc
	ds_write2_b32 v3, v4, v45 offset1:1
	v_add_u32_e32 v1, 0x200, v1
	s_mov_b64 exec, s[0:1]
	v_cmp_ge_u32_e32 vcc, v44, v0
	v_or_b32_e32 v4, 0x1d40, v129
	v_min_u32_e32 v3, v1, v5
	s_mov_b64 exec, vcc
	ds_write2_b32 v3, v4, v44 offset1:1
	v_add_u32_e32 v1, 0x200, v1
	s_mov_b64 exec, s[0:1]
	v_cmp_ge_u32_e32 vcc, v43, v0
	v_or_b32_e32 v4, 0x1d80, v129
	v_min_u32_e32 v3, v1, v5
	s_mov_b64 exec, vcc
	ds_write2_b32 v3, v4, v43 offset1:1
	v_add_u32_e32 v1, 0x200, v1
	s_mov_b64 exec, s[0:1]
	v_cmp_ge_u32_e32 vcc, v42, v0
	v_or_b32_e32 v4, 0x1dc0, v129
	v_min_u32_e32 v3, v1, v5
	s_mov_b64 exec, vcc
	ds_write2_b32 v3, v4, v42 offset1:1
	v_add_u32_e32 v1, 0x200, v1
	s_mov_b64 exec, s[0:1]
	v_cmp_ge_u32_e32 vcc, v41, v0
	v_or_b32_e32 v4, 0x1e00, v129
	v_min_u32_e32 v3, v1, v5
	s_mov_b64 exec, vcc
	ds_write2_b32 v3, v4, v41 offset1:1
	v_add_u32_e32 v1, 0x200, v1
	s_mov_b64 exec, s[0:1]
	v_cmp_ge_u32_e32 vcc, v40, v0
	v_or_b32_e32 v4, 0x1e40, v129
	v_min_u32_e32 v3, v1, v5
	s_mov_b64 exec, vcc
	ds_write2_b32 v3, v4, v40 offset1:1
	v_add_u32_e32 v1, 0x200, v1
	s_mov_b64 exec, s[0:1]
	v_cmp_ge_u32_e32 vcc, v39, v0
	v_or_b32_e32 v4, 0x1e80, v129
	v_min_u32_e32 v3, v1, v5
	s_mov_b64 exec, vcc
	ds_write2_b32 v3, v4, v39 offset1:1
	v_add_u32_e32 v1, 0x200, v1
	s_mov_b64 exec, s[0:1]
	v_cmp_ge_u32_e32 vcc, v38, v0
	v_or_b32_e32 v4, 0x1ec0, v129
	v_min_u32_e32 v3, v1, v5
	s_mov_b64 exec, vcc
	ds_write2_b32 v3, v4, v38 offset1:1
	v_add_u32_e32 v1, 0x200, v1
	s_mov_b64 exec, s[0:1]
	v_cmp_ge_u32_e32 vcc, v37, v0
	v_or_b32_e32 v4, 0x1f00, v129
	v_min_u32_e32 v3, v1, v5
	s_mov_b64 exec, vcc
	ds_write2_b32 v3, v4, v37 offset1:1
	v_add_u32_e32 v1, 0x200, v1
	s_mov_b64 exec, s[0:1]
	v_cmp_ge_u32_e32 vcc, v36, v0
	v_or_b32_e32 v4, 0x1f40, v129
	v_min_u32_e32 v3, v1, v5
	s_mov_b64 exec, vcc
	ds_write2_b32 v3, v4, v36 offset1:1
	v_add_u32_e32 v1, 0x200, v1
	s_mov_b64 exec, s[0:1]
	v_cmp_ge_u32_e32 vcc, v35, v0
	v_or_b32_e32 v4, 0x1f80, v129
	v_min_u32_e32 v3, v1, v5
	s_mov_b64 exec, vcc
	ds_write2_b32 v3, v4, v35 offset1:1
	v_add_u32_e32 v1, 0x200, v1
	s_mov_b64 exec, s[0:1]
	v_cmp_ge_u32_e32 vcc, v32, v0
	v_or_b32_e32 v4, 0x1fc0, v129
	v_min_u32_e32 v3, v1, v5
	s_mov_b64 exec, vcc
	ds_write2_b32 v3, v4, v32 offset1:1
	v_add_u32_e32 v1, 0x200, v1
	s_mov_b64 exec, s[0:1]
	v_sub_u32_e32 v3, v1, v6
	v_lshrrev_b32_e32 v3, 9, v3
	v_mov_b32_e32 v0, v251
	s_waitcnt lgkmcnt(0)
	s_mov_b64 s[0:1], -1
	v_lshlrev_b32_e32 v0, 2, v0
	v_mov_b32_e32 v1, v3
	s_nop 1
	v_max_i32_dpp v1, v1, v1 quad_perm:[1,0,3,2] row_mask:0xf bank_mask:0xf
	s_nop 1
	v_max_i32_dpp v1, v1, v1 quad_perm:[2,3,0,1] row_mask:0xf bank_mask:0xf
	s_nop 1
	v_max_i32_dpp v1, v1, v1 row_half_mirror row_mask:0xf bank_mask:0xf
	s_nop 1
	v_max_i32_dpp v1, v1, v1 row_mirror row_mask:0xf bank_mask:0xf
	v_mov_b32_e32 v0, v1
	v_mov_b32_e32 v4, v1
	s_nop 1
	v_permlane16_swap_b32 v0, v4
	v_max_i32_e32 v1, v0, v4
	v_mov_b32_e32 v0, v1
	v_mov_b32_e32 v4, v1
	s_nop 1
	v_permlane32_swap_b32 v0, v4
	v_max_i32_e32 v0, v0, v4
	s_nop 0
	v_readfirstlane_b32 s12, v0
	s_cmp_gt_i32 s12, 24
	s_cbranch_scc1 .LBB0_1271
	s_mov_b32 s20, 0
	s_cmp_lt_i32 s12, 1
	s_cbranch_scc1 .LBB0_1246
	v_mov_b32_e32 v4, v6
	s_mov_b32 s21, 0
	s_mov_b32 s13, 0
	ds_read_b64 v[186:187], v4
	s_branch .LBB0_1231
